# out-proj epilogue touch-prefetch extended to the f32 residual source of layer 0
# baseline (speedup 1.0000x reference)
.LBB0_1039:
	s_add_u32 s4, s36, 0xfff80080
	s_addc_u32 s5, s37, -1
	s_add_i32 s64, 0, 0x10000
	v_add_u32_e32 v142, s64, v179
	ds_read_b128 v[130:133], v142
	ds_read_b128 v[134:137], v142 offset:1024
	ds_read_b128 v[138:141], v142 offset:2048
	ds_read_b128 v[142:145], v142 offset:3072
	s_cmp_eq_u32 s92, 28
	s_cselect_b32 s55, s49, s5
	s_cselect_b32 s54, s89, s4
	s_cselect_b32 s5, s47, s24
	s_cselect_b32 s4, s14, s10
	v_lshl_add_u64 v[160:161], s[36:37], 0, v[152:153]
	s_add_i32 m0, s20, 0xc000
	ds_read_b128 v[156:159], v181
	ds_read_b128 v[174:177], v181 offset:1024
	ds_read_b128 v[182:185], v181 offset:2048
	ds_read_b128 v[186:189], v181 offset:3072
	ds_read_b128 v[190:193], v181 offset:4096
	ds_read_b128 v[194:197], v181 offset:5120
	ds_read_b128 v[198:201], v181 offset:6144
	ds_read_b128 v[206:209], v181 offset:7168
	global_load_lds_dwordx4 v[160:161], off
	v_lshl_add_u64 v[160:161], s[36:37], 0, v[154:155]
	s_add_i32 m0, s20, 0xe000
	s_nop 0
	global_load_lds_dwordx4 v[160:161], off
	s_waitcnt lgkmcnt(8)
	s_barrier
	s_waitcnt lgkmcnt(0)
	s_setprio 1
	s_waitcnt lgkmcnt(0)
	v_mfma_f32_16x16x32_bf16 v[126:129], v[130:133], v[156:159], v[126:129]
	v_mfma_f32_16x16x32_bf16 v[122:125], v[138:141], v[156:159], v[122:125]
	v_mfma_f32_16x16x32_bf16 v[110:113], v[130:133], v[182:185], v[110:113]
	v_mfma_f32_16x16x32_bf16 v[106:109], v[138:141], v[182:185], v[106:109]
	v_mfma_f32_16x16x32_bf16 v[92:95], v[130:133], v[190:193], v[92:95]
	v_mfma_f32_16x16x32_bf16 v[88:91], v[138:141], v[190:193], v[88:91]
	v_mfma_f32_16x16x32_bf16 v[76:79], v[130:133], v[198:201], v[76:79]
	v_mfma_f32_16x16x32_bf16 v[72:75], v[138:141], v[198:201], v[72:75]
	v_mfma_f32_16x16x32_bf16 v[126:129], v[134:137], v[174:177], v[126:129]
	v_mfma_f32_16x16x32_bf16 v[122:125], v[142:145], v[174:177], v[122:125]
	v_mfma_f32_16x16x32_bf16 v[110:113], v[134:137], v[186:189], v[110:113]
	v_mfma_f32_16x16x32_bf16 v[106:109], v[142:145], v[186:189], v[106:109]
	v_mfma_f32_16x16x32_bf16 v[92:95], v[134:137], v[194:197], v[92:95]
	v_mfma_f32_16x16x32_bf16 v[88:91], v[142:145], v[194:197], v[88:91]
	v_mfma_f32_16x16x32_bf16 v[76:79], v[134:137], v[206:209], v[76:79]
	v_mfma_f32_16x16x32_bf16 v[72:75], v[142:145], v[206:209], v[72:75]
	s_setprio 0
	s_barrier
	s_add_i32 s66, 0, 0x14000
	v_add_u32_e32 v160, s66, v179
	s_add_i32 s64, s64, s8
	ds_read_b128 v[228:231], v160
	ds_read_b128 v[232:235], v160 offset:1024
	ds_read_b128 v[236:239], v160 offset:2048
	ds_read_b128 v[240:243], v160 offset:3072
	v_lshl_add_u64 v[160:161], s[4:5], 0, v[96:97]
	s_mov_b32 m0, s64
	v_lshl_add_u64 v[202:203], s[4:5], 0, v[146:147]
	global_load_lds_dwordx4 v[160:161], off
	s_add_i32 m0, s64, 0x2000
	s_nop 0
	global_load_lds_dwordx4 v[202:203], off
	s_barrier
	s_waitcnt lgkmcnt(0)
	s_setprio 1
	s_waitcnt lgkmcnt(0)
	v_mfma_f32_16x16x32_bf16 v[118:121], v[228:231], v[156:159], v[118:121]
	v_mfma_f32_16x16x32_bf16 v[114:117], v[236:239], v[156:159], v[114:117]
	v_mfma_f32_16x16x32_bf16 v[102:105], v[228:231], v[182:185], v[102:105]
	v_mfma_f32_16x16x32_bf16 v[98:101], v[236:239], v[182:185], v[98:101]
	v_mfma_f32_16x16x32_bf16 v[84:87], v[228:231], v[190:193], v[84:87]
	v_mfma_f32_16x16x32_bf16 v[80:83], v[236:239], v[190:193], v[80:83]
	v_mfma_f32_16x16x32_bf16 v[68:71], v[228:231], v[198:201], v[68:71]
	v_mfma_f32_16x16x32_bf16 v[64:67], v[236:239], v[198:201], v[64:67]
	v_mfma_f32_16x16x32_bf16 v[118:121], v[232:235], v[174:177], v[118:121]
	v_mfma_f32_16x16x32_bf16 v[114:117], v[240:243], v[174:177], v[114:117]
	v_mfma_f32_16x16x32_bf16 v[102:105], v[232:235], v[186:189], v[102:105]
	v_mfma_f32_16x16x32_bf16 v[98:101], v[240:243], v[186:189], v[98:101]
	v_mfma_f32_16x16x32_bf16 v[84:87], v[232:235], v[194:197], v[84:87]
	v_mfma_f32_16x16x32_bf16 v[80:83], v[240:243], v[194:197], v[80:83]
	v_mfma_f32_16x16x32_bf16 v[68:71], v[232:235], v[206:209], v[68:71]
	v_mfma_f32_16x16x32_bf16 v[64:67], v[240:243], v[206:209], v[64:67]
	s_setprio 0
	s_mov_b32 m0, s20
	v_lshl_add_u64 v[212:213], s[54:55], 0, v[150:151]
	s_barrier
	ds_read_b128 v[156:159], v181 offset:16384
	ds_read_b128 v[174:177], v181 offset:17408
	ds_read_b128 v[182:185], v181 offset:18432
	ds_read_b128 v[186:189], v181 offset:19456
	ds_read_b128 v[190:193], v181 offset:20480
	ds_read_b128 v[194:197], v181 offset:21504
	ds_read_b128 v[198:201], v181 offset:22528
	ds_read_b128 v[206:209], v181 offset:23552
	global_load_lds_dwordx4 v[212:213], off
	v_lshl_add_u64 v[244:245], s[54:55], 0, v[148:149]
	s_mov_b32 m0, s21
	s_nop 0
	global_load_lds_dwordx4 v[244:245], off
	s_barrier
	s_waitcnt lgkmcnt(0)
	s_setprio 1
	s_waitcnt lgkmcnt(0)
	v_mfma_f32_16x16x32_bf16 v[60:63], v[130:133], v[156:159], v[60:63]
	v_mfma_f32_16x16x32_bf16 v[56:59], v[138:141], v[156:159], v[56:59]
	v_mfma_f32_16x16x32_bf16 v[44:47], v[130:133], v[182:185], v[44:47]
	v_mfma_f32_16x16x32_bf16 v[40:43], v[138:141], v[182:185], v[40:43]
	v_mfma_f32_16x16x32_bf16 v[28:31], v[130:133], v[190:193], v[28:31]
	v_mfma_f32_16x16x32_bf16 v[24:27], v[138:141], v[190:193], v[24:27]
	v_mfma_f32_16x16x32_bf16 v[12:15], v[130:133], v[198:201], v[12:15]
	v_mfma_f32_16x16x32_bf16 v[8:11], v[138:141], v[198:201], v[8:11]
	v_mfma_f32_16x16x32_bf16 v[60:63], v[134:137], v[174:177], v[60:63]
	v_mfma_f32_16x16x32_bf16 v[56:59], v[142:145], v[174:177], v[56:59]
	v_mfma_f32_16x16x32_bf16 v[44:47], v[134:137], v[186:189], v[44:47]
	v_mfma_f32_16x16x32_bf16 v[40:43], v[142:145], v[186:189], v[40:43]
	v_mfma_f32_16x16x32_bf16 v[28:31], v[134:137], v[194:197], v[28:31]
	v_mfma_f32_16x16x32_bf16 v[24:27], v[142:145], v[194:197], v[24:27]
	v_mfma_f32_16x16x32_bf16 v[12:15], v[134:137], v[206:209], v[12:15]
	v_mfma_f32_16x16x32_bf16 v[8:11], v[142:145], v[206:209], v[8:11]
	s_setprio 0
	s_barrier
	s_add_u32 s64, s4, 0x80000
	s_addc_u32 s65, s5, 0
	s_add_i32 s66, s66, s8
	v_lshl_add_u64 v[130:131], s[64:65], 0, v[96:97]
	s_mov_b32 m0, s66
	s_nop 0
	global_load_lds_dwordx4 v[130:131], off
	v_lshl_add_u64 v[130:131], s[64:65], 0, v[146:147]
	s_add_i32 m0, s66, 0x2000
	s_nop 0
	global_load_lds_dwordx4 v[130:131], off
	s_waitcnt vmcnt(6)
	s_barrier
	s_setprio 1
	v_mfma_f32_16x16x32_bf16 v[52:55], v[228:231], v[156:159], v[52:55]
	v_mfma_f32_16x16x32_bf16 v[48:51], v[236:239], v[156:159], v[48:51]
	v_mfma_f32_16x16x32_bf16 v[36:39], v[228:231], v[182:185], v[36:39]
	v_mfma_f32_16x16x32_bf16 v[32:35], v[236:239], v[182:185], v[32:35]
	v_mfma_f32_16x16x32_bf16 v[20:23], v[228:231], v[190:193], v[20:23]
	v_mfma_f32_16x16x32_bf16 v[16:19], v[236:239], v[190:193], v[16:19]
	v_mfma_f32_16x16x32_bf16 v[4:7], v[228:231], v[198:201], v[4:7]
	v_mfma_f32_16x16x32_bf16 v[0:3], v[236:239], v[198:201], v[0:3]
	v_mfma_f32_16x16x32_bf16 v[52:55], v[232:235], v[174:177], v[52:55]
	v_mfma_f32_16x16x32_bf16 v[48:51], v[240:243], v[174:177], v[48:51]
	v_mfma_f32_16x16x32_bf16 v[36:39], v[232:235], v[186:189], v[36:39]
	v_mfma_f32_16x16x32_bf16 v[32:35], v[240:243], v[186:189], v[32:35]
	v_mfma_f32_16x16x32_bf16 v[20:23], v[232:235], v[194:197], v[20:23]
	v_mfma_f32_16x16x32_bf16 v[16:19], v[240:243], v[194:197], v[16:19]
	v_mfma_f32_16x16x32_bf16 v[4:7], v[232:235], v[206:209], v[4:7]
	v_mfma_f32_16x16x32_bf16 v[0:3], v[240:243], v[206:209], v[0:3]
	s_setprio 0
	s_add_i32 s64, 0, 0x18000
	v_add_u32_e32 v142, s64, v179
	s_barrier
	ds_read_b128 v[130:133], v142
	ds_read_b128 v[134:137], v142 offset:1024
	ds_read_b128 v[138:141], v142 offset:2048
	ds_read_b128 v[142:145], v142 offset:3072
	s_add_u32 s54, s54, 0x80000
	s_addc_u32 s55, s55, 0
	s_mov_b32 m0, s38
	v_lshl_add_u64 v[228:229], s[54:55], 0, v[150:151]
	ds_read_b128 v[156:159], v181 offset:32768
	ds_read_b128 v[174:177], v181 offset:33792
	ds_read_b128 v[182:185], v181 offset:34816
	ds_read_b128 v[186:189], v181 offset:35840
	ds_read_b128 v[190:193], v181 offset:36864
	ds_read_b128 v[194:197], v181 offset:37888
	ds_read_b128 v[198:201], v181 offset:38912
	ds_read_b128 v[206:209], v181 offset:39936
	global_load_lds_dwordx4 v[228:229], off
	v_lshl_add_u64 v[228:229], s[54:55], 0, v[148:149]
	s_mov_b32 m0, s39
	s_nop 0
	global_load_lds_dwordx4 v[228:229], off
	s_waitcnt lgkmcnt(8)
	s_barrier
	s_waitcnt lgkmcnt(0)
	s_setprio 1
	s_waitcnt lgkmcnt(0)
	v_mfma_f32_16x16x32_bf16 v[126:129], v[130:133], v[156:159], v[126:129]
	v_mfma_f32_16x16x32_bf16 v[122:125], v[138:141], v[156:159], v[122:125]
	v_mfma_f32_16x16x32_bf16 v[110:113], v[130:133], v[182:185], v[110:113]
	v_mfma_f32_16x16x32_bf16 v[106:109], v[138:141], v[182:185], v[106:109]
	v_mfma_f32_16x16x32_bf16 v[92:95], v[130:133], v[190:193], v[92:95]
	v_mfma_f32_16x16x32_bf16 v[88:91], v[138:141], v[190:193], v[88:91]
	v_mfma_f32_16x16x32_bf16 v[76:79], v[130:133], v[198:201], v[76:79]
	v_mfma_f32_16x16x32_bf16 v[72:75], v[138:141], v[198:201], v[72:75]
	v_mfma_f32_16x16x32_bf16 v[126:129], v[134:137], v[174:177], v[126:129]
	v_mfma_f32_16x16x32_bf16 v[122:125], v[142:145], v[174:177], v[122:125]
	v_mfma_f32_16x16x32_bf16 v[110:113], v[134:137], v[186:189], v[110:113]
	v_mfma_f32_16x16x32_bf16 v[106:109], v[142:145], v[186:189], v[106:109]
	v_mfma_f32_16x16x32_bf16 v[92:95], v[134:137], v[194:197], v[92:95]
	v_mfma_f32_16x16x32_bf16 v[88:91], v[142:145], v[194:197], v[88:91]
	v_mfma_f32_16x16x32_bf16 v[76:79], v[134:137], v[206:209], v[76:79]
	v_mfma_f32_16x16x32_bf16 v[72:75], v[142:145], v[206:209], v[72:75]
	s_setprio 0
	s_barrier
	s_add_i32 s54, 0, 0x1c000
	s_add_i32 s55, s64, s8
	v_add_u32_e32 v204, s54, v179
	v_lshl_add_u64 v[160:161], v[160:161], 0, s[18:19]
	s_mov_b32 m0, s55
	ds_read_b128 v[228:231], v204
	ds_read_b128 v[232:235], v204 offset:1024
	ds_read_b128 v[236:239], v204 offset:2048
	ds_read_b128 v[240:243], v204 offset:3072
	global_load_lds_dwordx4 v[160:161], off
	v_lshl_add_u64 v[160:161], v[202:203], 0, s[18:19]
	s_add_i32 m0, s55, 0x2000
	s_nop 0
	global_load_lds_dwordx4 v[160:161], off
	s_barrier
	s_waitcnt lgkmcnt(0)
	s_setprio 1
	s_waitcnt lgkmcnt(0)
	v_mfma_f32_16x16x32_bf16 v[118:121], v[228:231], v[156:159], v[118:121]
	v_mfma_f32_16x16x32_bf16 v[114:117], v[236:239], v[156:159], v[114:117]
	v_mfma_f32_16x16x32_bf16 v[102:105], v[228:231], v[182:185], v[102:105]
	v_mfma_f32_16x16x32_bf16 v[98:101], v[236:239], v[182:185], v[98:101]
	v_mfma_f32_16x16x32_bf16 v[84:87], v[228:231], v[190:193], v[84:87]
	v_mfma_f32_16x16x32_bf16 v[80:83], v[236:239], v[190:193], v[80:83]
	v_mfma_f32_16x16x32_bf16 v[68:71], v[228:231], v[198:201], v[68:71]
	v_mfma_f32_16x16x32_bf16 v[64:67], v[236:239], v[198:201], v[64:67]
	v_mfma_f32_16x16x32_bf16 v[118:121], v[232:235], v[174:177], v[118:121]
	v_mfma_f32_16x16x32_bf16 v[114:117], v[240:243], v[174:177], v[114:117]
	v_mfma_f32_16x16x32_bf16 v[102:105], v[232:235], v[186:189], v[102:105]
	v_mfma_f32_16x16x32_bf16 v[98:101], v[240:243], v[186:189], v[98:101]
	v_mfma_f32_16x16x32_bf16 v[84:87], v[232:235], v[194:197], v[84:87]
	v_mfma_f32_16x16x32_bf16 v[80:83], v[240:243], v[194:197], v[80:83]
	v_mfma_f32_16x16x32_bf16 v[68:71], v[232:235], v[206:209], v[68:71]
	v_mfma_f32_16x16x32_bf16 v[64:67], v[240:243], v[206:209], v[64:67]
	s_setprio 0
	s_mov_b32 m0, s74
	v_lshl_add_u64 v[160:161], v[212:213], 0, s[18:19]
	s_barrier
	ds_read_b128 v[156:159], v181 offset:49152
	ds_read_b128 v[174:177], v181 offset:50176
	ds_read_b128 v[182:185], v181 offset:51200
	ds_read_b128 v[186:189], v181 offset:52224
	ds_read_b128 v[190:193], v181 offset:53248
	ds_read_b128 v[194:197], v181 offset:54272
	ds_read_b128 v[198:201], v181 offset:55296
	ds_read_b128 v[206:209], v181 offset:56320
	global_load_lds_dwordx4 v[160:161], off
	v_lshl_add_u64 v[160:161], v[244:245], 0, s[18:19]
	s_mov_b32 m0, s79
	s_nop 0
	global_load_lds_dwordx4 v[160:161], off
	s_barrier
	s_waitcnt lgkmcnt(0)
	s_setprio 1
	s_waitcnt lgkmcnt(0)
	v_mfma_f32_16x16x32_bf16 v[60:63], v[130:133], v[156:159], v[60:63]
	v_mfma_f32_16x16x32_bf16 v[56:59], v[138:141], v[156:159], v[56:59]
	v_mfma_f32_16x16x32_bf16 v[44:47], v[130:133], v[182:185], v[44:47]
	v_mfma_f32_16x16x32_bf16 v[40:43], v[138:141], v[182:185], v[40:43]
	v_mfma_f32_16x16x32_bf16 v[28:31], v[130:133], v[190:193], v[28:31]
	v_mfma_f32_16x16x32_bf16 v[24:27], v[138:141], v[190:193], v[24:27]
	v_mfma_f32_16x16x32_bf16 v[12:15], v[130:133], v[198:201], v[12:15]
	v_mfma_f32_16x16x32_bf16 v[8:11], v[138:141], v[198:201], v[8:11]
	v_mfma_f32_16x16x32_bf16 v[60:63], v[134:137], v[174:177], v[60:63]
	v_mfma_f32_16x16x32_bf16 v[56:59], v[142:145], v[174:177], v[56:59]
	v_mfma_f32_16x16x32_bf16 v[44:47], v[134:137], v[186:189], v[44:47]
	v_mfma_f32_16x16x32_bf16 v[40:43], v[142:145], v[186:189], v[40:43]
	v_mfma_f32_16x16x32_bf16 v[28:31], v[134:137], v[194:197], v[28:31]
	v_mfma_f32_16x16x32_bf16 v[24:27], v[142:145], v[194:197], v[24:27]
	v_mfma_f32_16x16x32_bf16 v[12:15], v[134:137], v[206:209], v[12:15]
	v_mfma_f32_16x16x32_bf16 v[8:11], v[142:145], v[206:209], v[8:11]
	s_setprio 0
	s_barrier
	s_add_u32 s4, s4, 0x80080
	s_addc_u32 s5, s5, 0
	s_add_i32 s54, s54, s8
	v_lshl_add_u64 v[130:131], s[4:5], 0, v[96:97]
	s_mov_b32 m0, s54
	s_nop 0
	global_load_lds_dwordx4 v[130:131], off
	v_lshl_add_u64 v[130:131], s[4:5], 0, v[146:147]
	s_add_i32 m0, s54, 0x2000
	s_nop 0
	global_load_lds_dwordx4 v[130:131], off
	s_waitcnt vmcnt(6)
	s_barrier
	s_setprio 1
	v_mfma_f32_16x16x32_bf16 v[52:55], v[228:231], v[156:159], v[52:55]
	v_mfma_f32_16x16x32_bf16 v[48:51], v[236:239], v[156:159], v[48:51]
	v_mfma_f32_16x16x32_bf16 v[36:39], v[228:231], v[182:185], v[36:39]
	v_mfma_f32_16x16x32_bf16 v[32:35], v[236:239], v[182:185], v[32:35]
	v_mfma_f32_16x16x32_bf16 v[20:23], v[228:231], v[190:193], v[20:23]
	v_mfma_f32_16x16x32_bf16 v[16:19], v[236:239], v[190:193], v[16:19]
	v_mfma_f32_16x16x32_bf16 v[4:7], v[228:231], v[198:201], v[4:7]
	v_mfma_f32_16x16x32_bf16 v[0:3], v[236:239], v[198:201], v[0:3]
	v_mfma_f32_16x16x32_bf16 v[52:55], v[232:235], v[174:177], v[52:55]
	v_mfma_f32_16x16x32_bf16 v[48:51], v[240:243], v[174:177], v[48:51]
	v_mfma_f32_16x16x32_bf16 v[36:39], v[232:235], v[186:189], v[36:39]
	v_mfma_f32_16x16x32_bf16 v[32:35], v[240:243], v[186:189], v[32:35]
	v_mfma_f32_16x16x32_bf16 v[20:23], v[232:235], v[194:197], v[20:23]
	v_mfma_f32_16x16x32_bf16 v[16:19], v[240:243], v[194:197], v[16:19]
	v_mfma_f32_16x16x32_bf16 v[4:7], v[232:235], v[206:209], v[4:7]
	v_mfma_f32_16x16x32_bf16 v[0:3], v[240:243], v[206:209], v[0:3]
	s_setprio 0
	s_add_i32 s92, s92, 2
	s_add_u32 s36, s36, 0x100
	s_addc_u32 s37, s37, 0
	s_add_u32 s10, s10, 0x100
	s_addc_u32 s24, s24, 0
	s_cmp_gt_u32 s92, 29
	s_barrier
	s_cbranch_scc0 .LBB0_1039
	s_lshl_b32 s4, s88, 8
	s_add_i32 s4, s4, s78
	v_or_b32_e32 v158, s4, v178
	s_ashr_i32 s4, s4, 13
	s_mul_hi_i32 s5, s4, 0x34000
	s_mul_i32 s4, s4, 0x34000
	v_lshl_or_b32 v156, s84, 8, v180
	s_add_u32 s4, s42, s4
	v_ashrrev_i32_e32 v157, 31, v156
	s_addc_u32 s5, s43, s5
	v_lshl_add_u64 v[160:161], v[156:157], 2, s[4:5]
	global_load_dwordx4 v[130:133], v[160:161], off offset:16
	global_load_dwordx4 v[134:137], v[160:161], off
	s_and_b64 vcc, exec, s[44:45]
	s_cbranch_vccnz .Lgpf_f32
	v_lshlrev_b32_e32 v228, 12, v158
	v_lshl_add_u32 v228, v156, 1, v228
	global_load_dword v237, v228, s[40:41]
	global_load_dword v237, v228, s[40:41] offset:256
	v_add_u32_e32 v230, 0x10000, v228
	global_load_dword v237, v230, s[40:41]
	global_load_dword v237, v230, s[40:41] offset:256
	v_add_u32_e32 v231, 0x20000, v228
	global_load_dword v237, v231, s[40:41]
	global_load_dword v237, v231, s[40:41] offset:256
	v_add_u32_e32 v232, 0x30000, v228
	global_load_dword v237, v232, s[40:41]
	global_load_dword v237, v232, s[40:41] offset:256
	v_add_u32_e32 v233, 0x80000, v228
	global_load_dword v237, v233, s[40:41]
	global_load_dword v237, v233, s[40:41] offset:256
	v_add_u32_e32 v234, 0x90000, v228
	global_load_dword v237, v234, s[40:41]
	global_load_dword v237, v234, s[40:41] offset:256
	v_add_u32_e32 v235, 0xa0000, v228
	global_load_dword v237, v235, s[40:41]
	global_load_dword v237, v235, s[40:41] offset:256
	v_add_u32_e32 v236, 0xb0000, v228
	global_load_dword v237, v236, s[40:41]
	global_load_dword v237, v236, s[40:41] offset:256
	s_branch .Lgpf_skip
.Lgpf_f32:
	v_lshlrev_b32_e32 v228, 13, v158
	v_lshl_add_u32 v228, v156, 2, v228
	global_load_dword v237, v228, s[28:29]
	global_load_dword v237, v228, s[28:29] offset:512
	v_add_u32_e32 v230, 0x20000, v228
	global_load_dword v237, v230, s[28:29]
	global_load_dword v237, v230, s[28:29] offset:512
	v_add_u32_e32 v231, 0x40000, v228
	global_load_dword v237, v231, s[28:29]
	global_load_dword v237, v231, s[28:29] offset:512
	v_add_u32_e32 v232, 0x60000, v228
	global_load_dword v237, v232, s[28:29]
	global_load_dword v237, v232, s[28:29] offset:512
	v_add_u32_e32 v233, 0x100000, v228
	global_load_dword v237, v233, s[28:29]
	global_load_dword v237, v233, s[28:29] offset:512
	v_add_u32_e32 v234, 0x120000, v228
	global_load_dword v237, v234, s[28:29]
	global_load_dword v237, v234, s[28:29] offset:512
	v_add_u32_e32 v235, 0x140000, v228
	global_load_dword v237, v235, s[28:29]
	global_load_dword v237, v235, s[28:29] offset:512
	v_add_u32_e32 v236, 0x160000, v228
	global_load_dword v237, v236, s[28:29]
	global_load_dword v237, v236, s[28:29] offset:512
